# out_proj epilogue: residual batch 1 waits counted per consumed pair (vmcnt 14..7) instead of one vmcnt(0)
# speedup vs baseline: 1.0034x; 1.0034x over previous
.LBB0_1396:
	s_add_i32 s19, s27, 0
	s_ashr_i32 s27, s26, 31
	s_add_i32 s19, s19, 0x25000
	s_lshl_b64 s[26:27], s[26:27], 19
	v_lshl_or_b32 v162, s75, 8, v231
	s_add_u32 s26, s66, s26
	v_lshlrev_b32_e32 v130, 2, v231
	s_addc_u32 s27, s67, s27
	s_andn2_b64 vcc, exec, s[16:17]
	v_add_u32_e32 v163, s19, v130
	v_add_u32_e32 v208, v162, v192
	s_cbranch_vccnz .LBB0_1402
	v_ashrrev_i32_e32 v209, 31, v208
	v_lshl_add_u64 v[130:131], v[208:209], 2, s[28:29]
	global_load_dwordx4 v[170:173], v[130:131], off nt
	global_load_dwordx4 v[174:177], v[130:131], off offset:16 nt
	global_load_dwordx4 v[178:181], v[130:131], off offset:512 nt
	global_load_dwordx4 v[182:185], v[130:131], off offset:528 nt
	v_add_u32_e32 v218, 0x4000, v208
	v_ashrrev_i32_e32 v219, 31, v218
	v_lshl_add_u64 v[130:131], v[218:219], 2, s[28:29]
	global_load_dwordx4 v[210:213], v[130:131], off offset:16 nt
	global_load_dwordx4 v[214:217], v[130:131], off nt
	v_add_u32_e32 v168, 0x4080, v208
	v_add_u32_e32 v166, 0x8000, v208
	v_add_u32_e32 v164, 0x8080, v208
	v_add_u32_e32 v160, 0xc000, v208
	v_add_u32_e32 v158, 0xc080, v208
	v_ashrrev_i32_e32 v169, 31, v168
	v_ashrrev_i32_e32 v167, 31, v166
	v_ashrrev_i32_e32 v165, 31, v164
	v_ashrrev_i32_e32 v161, 31, v160
	v_ashrrev_i32_e32 v159, 31, v158
	v_lshl_add_u64 v[130:131], v[168:169], 2, s[28:29]
	v_lshl_add_u64 v[132:133], v[166:167], 2, s[28:29]
	v_lshl_add_u64 v[134:135], v[164:165], 2, s[28:29]
	v_lshl_add_u64 v[136:137], v[160:161], 2, s[28:29]
	v_lshl_add_u64 v[238:239], v[158:159], 2, s[28:29]
	global_load_dwordx4 v[222:225], v[130:131], off offset:16 nt
	global_load_dwordx4 v[226:229], v[130:131], off nt
	global_load_dwordx4 v[154:157], v[132:133], off offset:16 nt
	global_load_dwordx4 v[234:237], v[132:133], off nt
	global_load_dwordx4 v[146:149], v[134:135], off offset:16 nt
	global_load_dwordx4 v[150:153], v[134:135], off nt
	global_load_dwordx4 v[138:141], v[136:137], off offset:16 nt
	global_load_dwordx4 v[142:145], v[136:137], off nt
	s_nop 0
	global_load_dwordx4 v[130:133], v[238:239], off offset:16 nt
	global_load_dwordx4 v[134:137], v[238:239], off nt
	ds_read_b128 v[238:241], v163
	ds_read_b128 v[242:245], v163 offset:1024
	v_lshl_add_u64 v[246:247], v[208:209], 1, s[26:27]
	v_lshl_add_u64 v[168:169], v[168:169], 1, s[26:27]
	v_lshl_add_u64 v[166:167], v[166:167], 1, s[26:27]
	s_waitcnt lgkmcnt(0)
	v_pk_add_f32 v[238:239], v[126:127], v[238:239]
	v_pk_add_f32 v[240:241], v[128:129], v[240:241]
	v_add_u32_e32 v248, 0x24000, v208
	v_ashrrev_i32_e32 v249, 31, v248
	s_waitcnt vmcnt(14)
	v_pk_fma_f32 v[170:171], v[242:243], v[238:239], v[170:171]
	v_pk_fma_f32 v[172:173], v[244:245], v[240:241], v[172:173]
	v_cvt_pk_bf16_f32 v170, v170, v171
	s_nop 0
	v_cvt_pk_bf16_f32 v171, v172, v173
	ds_read_b128 v[238:241], v163 offset:16
	ds_read_b128 v[242:245], v163 offset:1040
	s_waitcnt lgkmcnt(1)
	v_pk_add_f32 v[172:173], v[124:125], v[240:241]
	v_pk_add_f32 v[238:239], v[122:123], v[238:239]
	s_waitcnt lgkmcnt(0)
	v_pk_fma_f32 v[176:177], v[244:245], v[172:173], v[176:177]
	v_pk_fma_f32 v[172:173], v[242:243], v[238:239], v[174:175]
	s_nop 0
	v_cvt_pk_bf16_f32 v172, v172, v173
	v_cvt_pk_bf16_f32 v173, v176, v177
	global_store_dwordx4 v[246:247], v[170:173], off
	ds_read_b128 v[170:173], v163 offset:512
	ds_read_b128 v[174:177], v163 offset:1536
	s_waitcnt lgkmcnt(1)
	v_pk_add_f32 v[172:173], v[120:121], v[172:173]
	v_pk_add_f32 v[170:171], v[118:119], v[170:171]
	s_waitcnt lgkmcnt(0)
	s_waitcnt vmcnt(13)
	v_pk_fma_f32 v[172:173], v[176:177], v[172:173], v[180:181]
	v_pk_fma_f32 v[170:171], v[174:175], v[170:171], v[178:179]
	v_lshl_add_u64 v[180:181], v[218:219], 1, s[26:27]
	v_cvt_pk_bf16_f32 v170, v170, v171
	v_cvt_pk_bf16_f32 v171, v172, v173
	ds_read_b128 v[172:175], v163 offset:528
	ds_read_b128 v[176:179], v163 offset:1552
	v_add_u32_e32 v218, 0x20000, v208
	v_ashrrev_i32_e32 v219, 31, v218
	s_waitcnt lgkmcnt(1)
	v_pk_add_f32 v[172:173], v[114:115], v[172:173]
	v_pk_add_f32 v[174:175], v[116:117], v[174:175]
	s_waitcnt lgkmcnt(0)
	v_pk_fma_f32 v[172:173], v[176:177], v[172:173], v[182:183]
	v_pk_fma_f32 v[174:175], v[178:179], v[174:175], v[184:185]
	v_cvt_pk_bf16_f32 v172, v172, v173
	s_nop 0
	v_cvt_pk_bf16_f32 v173, v174, v175
	global_store_dwordx4 v[246:247], v[170:173], off offset:256
	ds_read_b128 v[170:173], v163
	ds_read_b128 v[174:177], v163 offset:1024
	v_add_u32_e32 v246, 0x20080, v208
	v_ashrrev_i32_e32 v247, 31, v246
	s_waitcnt lgkmcnt(1)
	v_pk_add_f32 v[172:173], v[112:113], v[172:173]
	v_pk_add_f32 v[170:171], v[110:111], v[170:171]
	s_waitcnt lgkmcnt(0)
	s_waitcnt vmcnt(12)
	v_pk_fma_f32 v[172:173], v[176:177], v[172:173], v[216:217]
	v_pk_fma_f32 v[170:171], v[174:175], v[170:171], v[214:215]
	s_nop 0
	v_cvt_pk_bf16_f32 v170, v170, v171
	v_cvt_pk_bf16_f32 v171, v172, v173
	ds_read_b128 v[172:175], v163 offset:16
	ds_read_b128 v[176:179], v163 offset:1040
	s_waitcnt lgkmcnt(1)
	v_pk_add_f32 v[172:173], v[106:107], v[172:173]
	v_pk_add_f32 v[174:175], v[108:109], v[174:175]
	s_waitcnt lgkmcnt(0)
	v_pk_fma_f32 v[172:173], v[176:177], v[172:173], v[210:211]
	v_pk_fma_f32 v[174:175], v[178:179], v[174:175], v[212:213]
	v_cvt_pk_bf16_f32 v172, v172, v173
	s_nop 0
	v_cvt_pk_bf16_f32 v173, v174, v175
	global_store_dwordx4 v[180:181], v[170:173], off
	ds_read_b128 v[170:173], v163 offset:512
	ds_read_b128 v[174:177], v163 offset:1536
	s_waitcnt lgkmcnt(1)
	v_pk_add_f32 v[172:173], v[104:105], v[172:173]
	v_pk_add_f32 v[170:171], v[102:103], v[170:171]
	s_waitcnt lgkmcnt(0)
	s_waitcnt vmcnt(11)
	v_pk_fma_f32 v[172:173], v[176:177], v[172:173], v[228:229]
	v_pk_fma_f32 v[170:171], v[174:175], v[170:171], v[226:227]
	s_nop 0
	v_cvt_pk_bf16_f32 v170, v170, v171
	v_cvt_pk_bf16_f32 v171, v172, v173
	ds_read_b128 v[172:175], v163 offset:528
	ds_read_b128 v[176:179], v163 offset:1552
	s_waitcnt lgkmcnt(1)
	v_pk_add_f32 v[172:173], v[98:99], v[172:173]
	v_pk_add_f32 v[174:175], v[100:101], v[174:175]
	s_waitcnt lgkmcnt(0)
	v_pk_fma_f32 v[172:173], v[176:177], v[172:173], v[222:223]
	v_pk_fma_f32 v[174:175], v[178:179], v[174:175], v[224:225]
	v_cvt_pk_bf16_f32 v172, v172, v173
	s_nop 0
	v_cvt_pk_bf16_f32 v173, v174, v175
	global_store_dwordx4 v[168:169], v[170:173], off
	ds_read_b128 v[168:171], v163
	ds_read_b128 v[172:175], v163 offset:1024
	s_waitcnt lgkmcnt(1)
	v_pk_add_f32 v[170:171], v[96:97], v[170:171]
	v_pk_add_f32 v[168:169], v[94:95], v[168:169]
	s_waitcnt lgkmcnt(0)
	s_waitcnt vmcnt(10)
	v_pk_fma_f32 v[170:171], v[174:175], v[170:171], v[236:237]
	v_pk_fma_f32 v[168:169], v[172:173], v[168:169], v[234:235]
	s_nop 0
	v_cvt_pk_bf16_f32 v168, v168, v169
	v_cvt_pk_bf16_f32 v169, v170, v171
	ds_read_b128 v[170:173], v163 offset:16
	ds_read_b128 v[174:177], v163 offset:1040
	s_waitcnt lgkmcnt(1)
	v_pk_add_f32 v[172:173], v[92:93], v[172:173]
	v_pk_add_f32 v[170:171], v[90:91], v[170:171]
	s_waitcnt lgkmcnt(0)
	v_pk_fma_f32 v[156:157], v[176:177], v[172:173], v[156:157]
	v_pk_fma_f32 v[154:155], v[174:175], v[170:171], v[154:155]
	s_nop 0
	v_cvt_pk_bf16_f32 v170, v154, v155
	v_cvt_pk_bf16_f32 v171, v156, v157
	global_store_dwordx4 v[166:167], v[168:171], off
	ds_read_b128 v[154:157], v163 offset:512
	ds_read_b128 v[166:169], v163 offset:1536
	s_waitcnt lgkmcnt(1)
	v_pk_add_f32 v[156:157], v[88:89], v[156:157]
	v_pk_add_f32 v[154:155], v[86:87], v[154:155]
	s_waitcnt lgkmcnt(0)
	s_waitcnt vmcnt(9)
	v_pk_fma_f32 v[152:153], v[168:169], v[156:157], v[152:153]
	v_pk_fma_f32 v[150:151], v[166:167], v[154:155], v[150:151]
	v_lshl_add_u64 v[156:157], v[164:165], 1, s[26:27]
	v_cvt_pk_bf16_f32 v150, v150, v151
	v_cvt_pk_bf16_f32 v151, v152, v153
	ds_read_b128 v[152:155], v163 offset:528
	ds_read_b128 v[166:169], v163 offset:1552
	v_add_u32_e32 v164, 0x28080, v208
	v_ashrrev_i32_e32 v165, 31, v164
	s_waitcnt lgkmcnt(1)
	v_pk_add_f32 v[154:155], v[84:85], v[154:155]
	v_pk_add_f32 v[152:153], v[82:83], v[152:153]
	s_waitcnt lgkmcnt(0)
	v_pk_fma_f32 v[148:149], v[168:169], v[154:155], v[148:149]
	v_pk_fma_f32 v[146:147], v[166:167], v[152:153], v[146:147]
	v_add_u32_e32 v168, 0x24080, v208
	v_cvt_pk_bf16_f32 v152, v146, v147
	v_cvt_pk_bf16_f32 v153, v148, v149
	global_store_dwordx4 v[156:157], v[150:153], off
	ds_read_b128 v[146:149], v163
	ds_read_b128 v[150:153], v163 offset:1024
	v_add_u32_e32 v166, 0x28000, v208
	v_ashrrev_i32_e32 v169, 31, v168
	v_ashrrev_i32_e32 v167, 31, v166
	s_waitcnt lgkmcnt(1)
	v_pk_add_f32 v[148:149], v[80:81], v[148:149]
	v_pk_add_f32 v[146:147], v[78:79], v[146:147]
	s_waitcnt lgkmcnt(0)
	s_waitcnt vmcnt(8)
	v_pk_fma_f32 v[144:145], v[152:153], v[148:149], v[144:145]
	v_pk_fma_f32 v[142:143], v[150:151], v[146:147], v[142:143]
	v_lshl_add_u64 v[152:153], v[160:161], 1, s[26:27]
	v_cvt_pk_bf16_f32 v142, v142, v143
	v_cvt_pk_bf16_f32 v143, v144, v145
	ds_read_b128 v[144:147], v163 offset:16
	ds_read_b128 v[148:151], v163 offset:1040
	v_add_u32_e32 v160, 0x2c000, v208
	v_ashrrev_i32_e32 v161, 31, v160
	s_waitcnt lgkmcnt(1)
	v_pk_add_f32 v[146:147], v[76:77], v[146:147]
	v_pk_add_f32 v[144:145], v[74:75], v[144:145]
	s_waitcnt lgkmcnt(0)
	v_pk_fma_f32 v[140:141], v[150:151], v[146:147], v[140:141]
	v_pk_fma_f32 v[138:139], v[148:149], v[144:145], v[138:139]
	v_lshl_add_u64 v[146:147], v[218:219], 2, s[28:29]
	v_cvt_pk_bf16_f32 v144, v138, v139
	v_cvt_pk_bf16_f32 v145, v140, v141
	global_store_dwordx4 v[152:153], v[142:145], off
	ds_read_b128 v[138:141], v163 offset:512
	ds_read_b128 v[142:145], v163 offset:1536
	v_lshl_add_u64 v[218:219], v[218:219], 1, s[26:27]
	s_waitcnt lgkmcnt(1)
	v_pk_add_f32 v[140:141], v[72:73], v[140:141]
	v_pk_add_f32 v[138:139], v[70:71], v[138:139]
	s_waitcnt lgkmcnt(0)
	s_waitcnt vmcnt(7)
	v_pk_fma_f32 v[136:137], v[144:145], v[140:141], v[136:137]
	v_pk_fma_f32 v[134:135], v[142:143], v[138:139], v[134:135]
	v_lshl_add_u64 v[144:145], v[158:159], 1, s[26:27]
	v_cvt_pk_bf16_f32 v134, v134, v135
	v_cvt_pk_bf16_f32 v135, v136, v137
	ds_read_b128 v[136:139], v163 offset:528
	ds_read_b128 v[140:143], v163 offset:1552
	v_add_u32_e32 v158, 0x2c080, v208
	v_ashrrev_i32_e32 v159, 31, v158
	v_lshl_add_u64 v[238:239], v[158:159], 2, s[28:29]
	s_waitcnt lgkmcnt(1)
	v_pk_add_f32 v[138:139], v[68:69], v[138:139]
	v_pk_add_f32 v[136:137], v[66:67], v[136:137]
	s_waitcnt lgkmcnt(0)
	v_pk_fma_f32 v[132:133], v[142:143], v[138:139], v[132:133]
	v_pk_fma_f32 v[130:131], v[140:141], v[136:137], v[130:131]
	s_nop 0
	v_cvt_pk_bf16_f32 v136, v130, v131
	v_cvt_pk_bf16_f32 v137, v132, v133
	global_store_dwordx4 v[144:145], v[134:137], off
	global_load_dwordx4 v[170:173], v[146:147], off nt
	global_load_dwordx4 v[174:177], v[146:147], off offset:16 nt
	v_lshl_add_u64 v[130:131], v[246:247], 2, s[28:29]
	global_load_dwordx4 v[178:181], v[130:131], off nt
	global_load_dwordx4 v[182:185], v[130:131], off offset:16 nt
	v_lshl_add_u64 v[130:131], v[248:249], 2, s[28:29]
	global_load_dwordx4 v[210:213], v[130:131], off offset:16 nt
	global_load_dwordx4 v[214:217], v[130:131], off nt
	v_lshl_add_u64 v[130:131], v[168:169], 2, s[28:29]
	v_lshl_add_u64 v[132:133], v[166:167], 2, s[28:29]
	v_lshl_add_u64 v[134:135], v[164:165], 2, s[28:29]
	v_lshl_add_u64 v[136:137], v[160:161], 2, s[28:29]
	global_load_dwordx4 v[222:225], v[130:131], off offset:16 nt
	global_load_dwordx4 v[226:229], v[130:131], off nt
	global_load_dwordx4 v[154:157], v[132:133], off offset:16 nt
	global_load_dwordx4 v[234:237], v[132:133], off nt
	global_load_dwordx4 v[146:149], v[134:135], off offset:16 nt
	global_load_dwordx4 v[150:153], v[134:135], off nt
	global_load_dwordx4 v[138:141], v[136:137], off offset:16 nt
	global_load_dwordx4 v[142:145], v[136:137], off nt
	s_nop 0
	global_load_dwordx4 v[130:133], v[238:239], off offset:16 nt
	global_load_dwordx4 v[134:137], v[238:239], off nt
	ds_read_b128 v[238:241], v163
	ds_read_b128 v[242:245], v163 offset:1024
	v_lshl_add_u64 v[168:169], v[168:169], 1, s[26:27]
	v_lshl_add_u64 v[166:167], v[166:167], 1, s[26:27]
	s_waitcnt lgkmcnt(1)
	v_pk_add_f32 v[238:239], v[62:63], v[238:239]
	v_pk_add_f32 v[240:241], v[64:65], v[240:241]
	s_waitcnt vmcnt(15) lgkmcnt(0)
	v_pk_fma_f32 v[170:171], v[242:243], v[238:239], v[170:171]
	v_pk_fma_f32 v[172:173], v[244:245], v[240:241], v[172:173]
	v_cvt_pk_bf16_f32 v170, v170, v171
	s_nop 0
	v_cvt_pk_bf16_f32 v171, v172, v173
	ds_read_b128 v[238:241], v163 offset:16
	ds_read_b128 v[242:245], v163 offset:1040
	s_waitcnt lgkmcnt(1)
	v_pk_add_f32 v[172:173], v[60:61], v[240:241]
	v_pk_add_f32 v[238:239], v[58:59], v[238:239]
	s_waitcnt vmcnt(14) lgkmcnt(0)
	v_pk_fma_f32 v[176:177], v[244:245], v[172:173], v[176:177]
	v_pk_fma_f32 v[172:173], v[242:243], v[238:239], v[174:175]
	s_nop 0
	v_cvt_pk_bf16_f32 v172, v172, v173
	v_cvt_pk_bf16_f32 v173, v176, v177
	global_store_dwordx4 v[218:219], v[170:173], off
	ds_read_b128 v[170:173], v163 offset:512
	ds_read_b128 v[174:177], v163 offset:1536
	s_waitcnt lgkmcnt(1)
	v_pk_add_f32 v[172:173], v[56:57], v[172:173]
	v_pk_add_f32 v[170:171], v[54:55], v[170:171]
	s_waitcnt vmcnt(14) lgkmcnt(0)
	v_pk_fma_f32 v[172:173], v[176:177], v[172:173], v[180:181]
	v_pk_fma_f32 v[170:171], v[174:175], v[170:171], v[178:179]
	v_lshl_add_u64 v[180:181], v[246:247], 1, s[26:27]
	v_cvt_pk_bf16_f32 v170, v170, v171
	v_cvt_pk_bf16_f32 v171, v172, v173
	ds_read_b128 v[172:175], v163 offset:528
	ds_read_b128 v[176:179], v163 offset:1552
	s_waitcnt lgkmcnt(1)
	v_pk_add_f32 v[172:173], v[50:51], v[172:173]
	v_pk_add_f32 v[174:175], v[52:53], v[174:175]
	s_waitcnt vmcnt(13) lgkmcnt(0)
	v_pk_fma_f32 v[172:173], v[176:177], v[172:173], v[182:183]
	v_pk_fma_f32 v[174:175], v[178:179], v[174:175], v[184:185]
	v_cvt_pk_bf16_f32 v172, v172, v173
	s_nop 0
	v_cvt_pk_bf16_f32 v173, v174, v175
	global_store_dwordx4 v[180:181], v[170:173], off
	ds_read_b128 v[170:173], v163
	ds_read_b128 v[174:177], v163 offset:1024
	v_lshl_add_u64 v[180:181], v[248:249], 1, s[26:27]
	s_waitcnt lgkmcnt(1)
	v_pk_add_f32 v[172:173], v[48:49], v[172:173]
	v_pk_add_f32 v[170:171], v[46:47], v[170:171]
	s_waitcnt vmcnt(12) lgkmcnt(0)
	v_pk_fma_f32 v[172:173], v[176:177], v[172:173], v[216:217]
	v_pk_fma_f32 v[170:171], v[174:175], v[170:171], v[214:215]
	s_nop 0
	v_cvt_pk_bf16_f32 v170, v170, v171
	v_cvt_pk_bf16_f32 v171, v172, v173
	ds_read_b128 v[172:175], v163 offset:16
	ds_read_b128 v[176:179], v163 offset:1040
	s_waitcnt lgkmcnt(1)
	v_pk_add_f32 v[172:173], v[42:43], v[172:173]
	v_pk_add_f32 v[174:175], v[44:45], v[174:175]
	s_waitcnt lgkmcnt(0)
	v_pk_fma_f32 v[172:173], v[176:177], v[172:173], v[210:211]
	v_pk_fma_f32 v[174:175], v[178:179], v[174:175], v[212:213]
	v_cvt_pk_bf16_f32 v172, v172, v173
	s_nop 0
	v_cvt_pk_bf16_f32 v173, v174, v175
	global_store_dwordx4 v[180:181], v[170:173], off
	ds_read_b128 v[170:173], v163 offset:512
	ds_read_b128 v[174:177], v163 offset:1536
	s_waitcnt lgkmcnt(1)
	v_pk_add_f32 v[172:173], v[40:41], v[172:173]
	v_pk_add_f32 v[170:171], v[38:39], v[170:171]
	s_waitcnt vmcnt(11) lgkmcnt(0)
	v_pk_fma_f32 v[172:173], v[176:177], v[172:173], v[228:229]
	v_pk_fma_f32 v[170:171], v[174:175], v[170:171], v[226:227]
	s_nop 0
	v_cvt_pk_bf16_f32 v170, v170, v171
	v_cvt_pk_bf16_f32 v171, v172, v173
	ds_read_b128 v[172:175], v163 offset:528
	ds_read_b128 v[176:179], v163 offset:1552
	s_waitcnt lgkmcnt(1)
	v_pk_add_f32 v[172:173], v[34:35], v[172:173]
	v_pk_add_f32 v[174:175], v[36:37], v[174:175]
	s_waitcnt lgkmcnt(0)
	v_pk_fma_f32 v[172:173], v[176:177], v[172:173], v[222:223]
	v_pk_fma_f32 v[174:175], v[178:179], v[174:175], v[224:225]
	v_cvt_pk_bf16_f32 v172, v172, v173
	s_nop 0
	v_cvt_pk_bf16_f32 v173, v174, v175
	global_store_dwordx4 v[168:169], v[170:173], off
	ds_read_b128 v[168:171], v163
	ds_read_b128 v[172:175], v163 offset:1024
	s_waitcnt lgkmcnt(1)
	v_pk_add_f32 v[170:171], v[32:33], v[170:171]
	v_pk_add_f32 v[168:169], v[30:31], v[168:169]
	s_waitcnt vmcnt(10) lgkmcnt(0)
	v_pk_fma_f32 v[170:171], v[174:175], v[170:171], v[236:237]
	v_pk_fma_f32 v[168:169], v[172:173], v[168:169], v[234:235]
	s_nop 0
	v_cvt_pk_bf16_f32 v168, v168, v169
	v_cvt_pk_bf16_f32 v169, v170, v171
	ds_read_b128 v[170:173], v163 offset:16
	ds_read_b128 v[174:177], v163 offset:1040
	s_waitcnt lgkmcnt(1)
	v_pk_add_f32 v[172:173], v[28:29], v[172:173]
	v_pk_add_f32 v[170:171], v[26:27], v[170:171]
	s_waitcnt lgkmcnt(0)
	v_pk_fma_f32 v[156:157], v[176:177], v[172:173], v[156:157]
	v_pk_fma_f32 v[154:155], v[174:175], v[170:171], v[154:155]
	s_nop 0
	v_cvt_pk_bf16_f32 v170, v154, v155
	v_cvt_pk_bf16_f32 v171, v156, v157
	global_store_dwordx4 v[166:167], v[168:171], off
	ds_read_b128 v[154:157], v163 offset:512
	ds_read_b128 v[166:169], v163 offset:1536
	s_waitcnt lgkmcnt(1)
	v_pk_add_f32 v[156:157], v[24:25], v[156:157]
	v_pk_add_f32 v[154:155], v[22:23], v[154:155]
	s_waitcnt vmcnt(9) lgkmcnt(0)
	v_pk_fma_f32 v[152:153], v[168:169], v[156:157], v[152:153]
	v_pk_fma_f32 v[150:151], v[166:167], v[154:155], v[150:151]
	v_lshl_add_u64 v[156:157], v[164:165], 1, s[26:27]
	v_cvt_pk_bf16_f32 v150, v150, v151
	v_cvt_pk_bf16_f32 v151, v152, v153
	ds_read_b128 v[152:155], v163 offset:528
	ds_read_b128 v[166:169], v163 offset:1552
	s_waitcnt lgkmcnt(1)
	v_pk_add_f32 v[154:155], v[20:21], v[154:155]
	v_pk_add_f32 v[152:153], v[18:19], v[152:153]
	s_waitcnt lgkmcnt(0)
	v_pk_fma_f32 v[148:149], v[168:169], v[154:155], v[148:149]
	v_pk_fma_f32 v[146:147], v[166:167], v[152:153], v[146:147]
	s_nop 0
	v_cvt_pk_bf16_f32 v152, v146, v147
	v_cvt_pk_bf16_f32 v153, v148, v149
	global_store_dwordx4 v[156:157], v[150:153], off
	ds_read_b128 v[146:149], v163
	ds_read_b128 v[150:153], v163 offset:1024
	s_waitcnt lgkmcnt(1)
	v_pk_add_f32 v[148:149], v[16:17], v[148:149]
	v_pk_add_f32 v[146:147], v[14:15], v[146:147]
	s_waitcnt vmcnt(8) lgkmcnt(0)
	v_pk_fma_f32 v[144:145], v[152:153], v[148:149], v[144:145]
	v_pk_fma_f32 v[142:143], v[150:151], v[146:147], v[142:143]
	v_lshl_add_u64 v[152:153], v[160:161], 1, s[26:27]
	v_cvt_pk_bf16_f32 v142, v142, v143
	v_cvt_pk_bf16_f32 v143, v144, v145
	ds_read_b128 v[144:147], v163 offset:16
	ds_read_b128 v[148:151], v163 offset:1040
	s_waitcnt lgkmcnt(1)
	v_pk_add_f32 v[146:147], v[12:13], v[146:147]
	v_pk_add_f32 v[144:145], v[10:11], v[144:145]
	s_waitcnt lgkmcnt(0)
	v_pk_fma_f32 v[140:141], v[150:151], v[146:147], v[140:141]
	v_pk_fma_f32 v[138:139], v[148:149], v[144:145], v[138:139]
	s_nop 0
	v_cvt_pk_bf16_f32 v144, v138, v139
	v_cvt_pk_bf16_f32 v145, v140, v141
	global_store_dwordx4 v[152:153], v[142:145], off
	ds_read_b128 v[138:141], v163 offset:512
	ds_read_b128 v[142:145], v163 offset:1536
	s_waitcnt lgkmcnt(1)
	v_pk_add_f32 v[140:141], v[8:9], v[140:141]
	v_pk_add_f32 v[138:139], v[6:7], v[138:139]
	s_waitcnt vmcnt(7) lgkmcnt(0)
	v_pk_fma_f32 v[136:137], v[144:145], v[140:141], v[136:137]
	v_pk_fma_f32 v[134:135], v[142:143], v[138:139], v[134:135]
	s_nop 0
	v_cvt_pk_bf16_f32 v134, v134, v135
	v_cvt_pk_bf16_f32 v135, v136, v137
	ds_read_b128 v[136:139], v163 offset:528
	ds_read_b128 v[140:143], v163 offset:1552
	s_waitcnt lgkmcnt(1)
	v_pk_add_f32 v[138:139], v[4:5], v[138:139]
	v_pk_add_f32 v[136:137], v[2:3], v[136:137]
	s_waitcnt lgkmcnt(0)
	v_pk_fma_f32 v[132:133], v[142:143], v[138:139], v[132:133]
	v_pk_fma_f32 v[130:131], v[140:141], v[136:137], v[130:131]
	s_nop 0
	v_cvt_pk_bf16_f32 v136, v130, v131
	v_cvt_pk_bf16_f32 v137, v132, v133
	s_cbranch_execnz .LBB0_1399
